# v2 + P3 retention state scan: 16 loads in flight per buffer, double-buffered (compiler loop had 2 in flight due to store/load aliasing)
# speedup vs baseline: 1.0147x; 1.0147x over previous
.LBB0_527:
	v_lshlrev_b32_e32 v9, 2, v194
	s_add_u32 s14, s82, 0x50200000
	s_addc_u32 s15, s83, 0
	s_add_u32 s16, s82, 0x54200000
	s_addc_u32 s17, s83, 0
	s_mov_b32 s8, 0
	global_load_dword v20, v9, s[14:15]
	s_add_u32 s14, s14, 0x40000
	s_addc_u32 s15, s15, 0
	global_load_dword v21, v9, s[14:15]
	s_add_u32 s14, s14, 0x40000
	s_addc_u32 s15, s15, 0
	global_load_dword v22, v9, s[14:15]
	s_add_u32 s14, s14, 0x40000
	s_addc_u32 s15, s15, 0
	global_load_dword v23, v9, s[14:15]
	s_add_u32 s14, s14, 0x40000
	s_addc_u32 s15, s15, 0
	global_load_dword v24, v9, s[14:15]
	s_add_u32 s14, s14, 0x40000
	s_addc_u32 s15, s15, 0
	global_load_dword v25, v9, s[14:15]
	s_add_u32 s14, s14, 0x40000
	s_addc_u32 s15, s15, 0
	global_load_dword v26, v9, s[14:15]
	s_add_u32 s14, s14, 0x40000
	s_addc_u32 s15, s15, 0
	global_load_dword v27, v9, s[14:15]
	s_add_u32 s14, s14, 0x40000
	s_addc_u32 s15, s15, 0
	global_load_dword v28, v9, s[14:15]
	s_add_u32 s14, s14, 0x40000
	s_addc_u32 s15, s15, 0
	global_load_dword v29, v9, s[14:15]
	s_add_u32 s14, s14, 0x40000
	s_addc_u32 s15, s15, 0
	global_load_dword v30, v9, s[14:15]
	s_add_u32 s14, s14, 0x40000
	s_addc_u32 s15, s15, 0
	global_load_dword v31, v9, s[14:15]
	s_add_u32 s14, s14, 0x40000
	s_addc_u32 s15, s15, 0
	global_load_dword v32, v9, s[14:15]
	s_add_u32 s14, s14, 0x40000
	s_addc_u32 s15, s15, 0
	global_load_dword v33, v9, s[14:15]
	s_add_u32 s14, s14, 0x40000
	s_addc_u32 s15, s15, 0
	global_load_dword v34, v9, s[14:15]
	s_add_u32 s14, s14, 0x40000
	s_addc_u32 s15, s15, 0
	global_load_dword v35, v9, s[14:15]
	s_add_u32 s14, s14, 0x40000
	s_addc_u32 s15, s15, 0
.Lrs_loop:
	global_load_dword v36, v9, s[14:15]
	s_add_u32 s14, s14, 0x40000
	s_addc_u32 s15, s15, 0
	global_load_dword v37, v9, s[14:15]
	s_add_u32 s14, s14, 0x40000
	s_addc_u32 s15, s15, 0
	global_load_dword v38, v9, s[14:15]
	s_add_u32 s14, s14, 0x40000
	s_addc_u32 s15, s15, 0
	global_load_dword v39, v9, s[14:15]
	s_add_u32 s14, s14, 0x40000
	s_addc_u32 s15, s15, 0
	global_load_dword v40, v9, s[14:15]
	s_add_u32 s14, s14, 0x40000
	s_addc_u32 s15, s15, 0
	global_load_dword v41, v9, s[14:15]
	s_add_u32 s14, s14, 0x40000
	s_addc_u32 s15, s15, 0
	global_load_dword v42, v9, s[14:15]
	s_add_u32 s14, s14, 0x40000
	s_addc_u32 s15, s15, 0
	global_load_dword v43, v9, s[14:15]
	s_add_u32 s14, s14, 0x40000
	s_addc_u32 s15, s15, 0
	global_load_dword v44, v9, s[14:15]
	s_add_u32 s14, s14, 0x40000
	s_addc_u32 s15, s15, 0
	global_load_dword v45, v9, s[14:15]
	s_add_u32 s14, s14, 0x40000
	s_addc_u32 s15, s15, 0
	global_load_dword v46, v9, s[14:15]
	s_add_u32 s14, s14, 0x40000
	s_addc_u32 s15, s15, 0
	global_load_dword v47, v9, s[14:15]
	s_add_u32 s14, s14, 0x40000
	s_addc_u32 s15, s15, 0
	global_load_dword v48, v9, s[14:15]
	s_add_u32 s14, s14, 0x40000
	s_addc_u32 s15, s15, 0
	global_load_dword v49, v9, s[14:15]
	s_add_u32 s14, s14, 0x40000
	s_addc_u32 s15, s15, 0
	global_load_dword v50, v9, s[14:15]
	s_add_u32 s14, s14, 0x40000
	s_addc_u32 s15, s15, 0
	global_load_dword v51, v9, s[14:15]
	s_add_u32 s14, s14, 0x40000
	s_addc_u32 s15, s15, 0
	v_bfe_u32 v16, v13, 16, 1
	v_bfe_u32 v17, v12, 16, 1
	v_add3_u32 v16, v13, v16, s12
	v_add3_u32 v17, v12, v17, s12
	v_lshrrev_b32_e32 v16, 16, v16
	v_and_or_b32 v16, v17, s13, v16
	global_store_dword v9, v16, s[16:17]
	s_add_u32 s16, s16, 0x40000
	s_addc_u32 s17, s17, 0
	s_waitcnt vmcnt(32)
	v_lshlrev_b32_e32 v19, 16, v20
	v_and_b32_e32 v18, 0xffff0000, v20
	v_pk_fma_f32 v[12:13], v[6:7], v[12:13], v[18:19]
	v_bfe_u32 v10, v13, 16, 1
	v_bfe_u32 v11, v12, 16, 1
	v_add3_u32 v10, v13, v10, s12
	v_add3_u32 v11, v12, v11, s12
	v_lshrrev_b32_e32 v10, 16, v10
	v_and_or_b32 v10, v11, s13, v10
	global_store_dword v9, v10, s[16:17]
	s_add_u32 s16, s16, 0x40000
	s_addc_u32 s17, s17, 0
	s_waitcnt vmcnt(32)
	v_lshlrev_b32_e32 v19, 16, v21
	v_and_b32_e32 v18, 0xffff0000, v21
	v_pk_fma_f32 v[12:13], v[6:7], v[12:13], v[18:19]
	v_bfe_u32 v16, v13, 16, 1
	v_bfe_u32 v17, v12, 16, 1
	v_add3_u32 v16, v13, v16, s12
	v_add3_u32 v17, v12, v17, s12
	v_lshrrev_b32_e32 v16, 16, v16
	v_and_or_b32 v16, v17, s13, v16
	global_store_dword v9, v16, s[16:17]
	s_add_u32 s16, s16, 0x40000
	s_addc_u32 s17, s17, 0
	s_waitcnt vmcnt(32)
	v_lshlrev_b32_e32 v19, 16, v22
	v_and_b32_e32 v18, 0xffff0000, v22
	v_pk_fma_f32 v[12:13], v[6:7], v[12:13], v[18:19]
	v_bfe_u32 v10, v13, 16, 1
	v_bfe_u32 v11, v12, 16, 1
	v_add3_u32 v10, v13, v10, s12
	v_add3_u32 v11, v12, v11, s12
	v_lshrrev_b32_e32 v10, 16, v10
	v_and_or_b32 v10, v11, s13, v10
	global_store_dword v9, v10, s[16:17]
	s_add_u32 s16, s16, 0x40000
	s_addc_u32 s17, s17, 0
	s_waitcnt vmcnt(32)
	v_lshlrev_b32_e32 v19, 16, v23
	v_and_b32_e32 v18, 0xffff0000, v23
	v_pk_fma_f32 v[12:13], v[6:7], v[12:13], v[18:19]
	v_bfe_u32 v16, v13, 16, 1
	v_bfe_u32 v17, v12, 16, 1
	v_add3_u32 v16, v13, v16, s12
	v_add3_u32 v17, v12, v17, s12
	v_lshrrev_b32_e32 v16, 16, v16
	v_and_or_b32 v16, v17, s13, v16
	global_store_dword v9, v16, s[16:17]
	s_add_u32 s16, s16, 0x40000
	s_addc_u32 s17, s17, 0
	s_waitcnt vmcnt(32)
	v_lshlrev_b32_e32 v19, 16, v24
	v_and_b32_e32 v18, 0xffff0000, v24
	v_pk_fma_f32 v[12:13], v[6:7], v[12:13], v[18:19]
	v_bfe_u32 v10, v13, 16, 1
	v_bfe_u32 v11, v12, 16, 1
	v_add3_u32 v10, v13, v10, s12
	v_add3_u32 v11, v12, v11, s12
	v_lshrrev_b32_e32 v10, 16, v10
	v_and_or_b32 v10, v11, s13, v10
	global_store_dword v9, v10, s[16:17]
	s_add_u32 s16, s16, 0x40000
	s_addc_u32 s17, s17, 0
	s_waitcnt vmcnt(32)
	v_lshlrev_b32_e32 v19, 16, v25
	v_and_b32_e32 v18, 0xffff0000, v25
	v_pk_fma_f32 v[12:13], v[6:7], v[12:13], v[18:19]
	v_bfe_u32 v16, v13, 16, 1
	v_bfe_u32 v17, v12, 16, 1
	v_add3_u32 v16, v13, v16, s12
	v_add3_u32 v17, v12, v17, s12
	v_lshrrev_b32_e32 v16, 16, v16
	v_and_or_b32 v16, v17, s13, v16
	global_store_dword v9, v16, s[16:17]
	s_add_u32 s16, s16, 0x40000
	s_addc_u32 s17, s17, 0
	s_waitcnt vmcnt(32)
	v_lshlrev_b32_e32 v19, 16, v26
	v_and_b32_e32 v18, 0xffff0000, v26
	v_pk_fma_f32 v[12:13], v[6:7], v[12:13], v[18:19]
	v_bfe_u32 v10, v13, 16, 1
	v_bfe_u32 v11, v12, 16, 1
	v_add3_u32 v10, v13, v10, s12
	v_add3_u32 v11, v12, v11, s12
	v_lshrrev_b32_e32 v10, 16, v10
	v_and_or_b32 v10, v11, s13, v10
	global_store_dword v9, v10, s[16:17]
	s_add_u32 s16, s16, 0x40000
	s_addc_u32 s17, s17, 0
	s_waitcnt vmcnt(32)
	v_lshlrev_b32_e32 v19, 16, v27
	v_and_b32_e32 v18, 0xffff0000, v27
	v_pk_fma_f32 v[12:13], v[6:7], v[12:13], v[18:19]
	v_bfe_u32 v16, v13, 16, 1
	v_bfe_u32 v17, v12, 16, 1
	v_add3_u32 v16, v13, v16, s12
	v_add3_u32 v17, v12, v17, s12
	v_lshrrev_b32_e32 v16, 16, v16
	v_and_or_b32 v16, v17, s13, v16
	global_store_dword v9, v16, s[16:17]
	s_add_u32 s16, s16, 0x40000
	s_addc_u32 s17, s17, 0
	s_waitcnt vmcnt(32)
	v_lshlrev_b32_e32 v19, 16, v28
	v_and_b32_e32 v18, 0xffff0000, v28
	v_pk_fma_f32 v[12:13], v[6:7], v[12:13], v[18:19]
	v_bfe_u32 v10, v13, 16, 1
	v_bfe_u32 v11, v12, 16, 1
	v_add3_u32 v10, v13, v10, s12
	v_add3_u32 v11, v12, v11, s12
	v_lshrrev_b32_e32 v10, 16, v10
	v_and_or_b32 v10, v11, s13, v10
	global_store_dword v9, v10, s[16:17]
	s_add_u32 s16, s16, 0x40000
	s_addc_u32 s17, s17, 0
	s_waitcnt vmcnt(32)
	v_lshlrev_b32_e32 v19, 16, v29
	v_and_b32_e32 v18, 0xffff0000, v29
	v_pk_fma_f32 v[12:13], v[6:7], v[12:13], v[18:19]
	v_bfe_u32 v16, v13, 16, 1
	v_bfe_u32 v17, v12, 16, 1
	v_add3_u32 v16, v13, v16, s12
	v_add3_u32 v17, v12, v17, s12
	v_lshrrev_b32_e32 v16, 16, v16
	v_and_or_b32 v16, v17, s13, v16
	global_store_dword v9, v16, s[16:17]
	s_add_u32 s16, s16, 0x40000
	s_addc_u32 s17, s17, 0
	s_waitcnt vmcnt(32)
	v_lshlrev_b32_e32 v19, 16, v30
	v_and_b32_e32 v18, 0xffff0000, v30
	v_pk_fma_f32 v[12:13], v[6:7], v[12:13], v[18:19]
	v_bfe_u32 v10, v13, 16, 1
	v_bfe_u32 v11, v12, 16, 1
	v_add3_u32 v10, v13, v10, s12
	v_add3_u32 v11, v12, v11, s12
	v_lshrrev_b32_e32 v10, 16, v10
	v_and_or_b32 v10, v11, s13, v10
	global_store_dword v9, v10, s[16:17]
	s_add_u32 s16, s16, 0x40000
	s_addc_u32 s17, s17, 0
	s_waitcnt vmcnt(32)
	v_lshlrev_b32_e32 v19, 16, v31
	v_and_b32_e32 v18, 0xffff0000, v31
	v_pk_fma_f32 v[12:13], v[6:7], v[12:13], v[18:19]
	v_bfe_u32 v16, v13, 16, 1
	v_bfe_u32 v17, v12, 16, 1
	v_add3_u32 v16, v13, v16, s12
	v_add3_u32 v17, v12, v17, s12
	v_lshrrev_b32_e32 v16, 16, v16
	v_and_or_b32 v16, v17, s13, v16
	global_store_dword v9, v16, s[16:17]
	s_add_u32 s16, s16, 0x40000
	s_addc_u32 s17, s17, 0
	s_waitcnt vmcnt(32)
	v_lshlrev_b32_e32 v19, 16, v32
	v_and_b32_e32 v18, 0xffff0000, v32
	v_pk_fma_f32 v[12:13], v[6:7], v[12:13], v[18:19]
	v_bfe_u32 v10, v13, 16, 1
	v_bfe_u32 v11, v12, 16, 1
	v_add3_u32 v10, v13, v10, s12
	v_add3_u32 v11, v12, v11, s12
	v_lshrrev_b32_e32 v10, 16, v10
	v_and_or_b32 v10, v11, s13, v10
	global_store_dword v9, v10, s[16:17]
	s_add_u32 s16, s16, 0x40000
	s_addc_u32 s17, s17, 0
	s_waitcnt vmcnt(32)
	v_lshlrev_b32_e32 v19, 16, v33
	v_and_b32_e32 v18, 0xffff0000, v33
	v_pk_fma_f32 v[12:13], v[6:7], v[12:13], v[18:19]
	v_bfe_u32 v16, v13, 16, 1
	v_bfe_u32 v17, v12, 16, 1
	v_add3_u32 v16, v13, v16, s12
	v_add3_u32 v17, v12, v17, s12
	v_lshrrev_b32_e32 v16, 16, v16
	v_and_or_b32 v16, v17, s13, v16
	global_store_dword v9, v16, s[16:17]
	s_add_u32 s16, s16, 0x40000
	s_addc_u32 s17, s17, 0
	s_waitcnt vmcnt(32)
	v_lshlrev_b32_e32 v19, 16, v34
	v_and_b32_e32 v18, 0xffff0000, v34
	v_pk_fma_f32 v[12:13], v[6:7], v[12:13], v[18:19]
	v_bfe_u32 v10, v13, 16, 1
	v_bfe_u32 v11, v12, 16, 1
	v_add3_u32 v10, v13, v10, s12
	v_add3_u32 v11, v12, v11, s12
	v_lshrrev_b32_e32 v10, 16, v10
	v_and_or_b32 v10, v11, s13, v10
	global_store_dword v9, v10, s[16:17]
	s_add_u32 s16, s16, 0x40000
	s_addc_u32 s17, s17, 0
	s_waitcnt vmcnt(32)
	v_lshlrev_b32_e32 v19, 16, v35
	v_and_b32_e32 v18, 0xffff0000, v35
	v_pk_fma_f32 v[12:13], v[6:7], v[12:13], v[18:19]
	s_cmp_eq_u32 s8, 3
	s_cbranch_scc1 .Lrs_last
	global_load_dword v20, v9, s[14:15]
	s_add_u32 s14, s14, 0x40000
	s_addc_u32 s15, s15, 0
	global_load_dword v21, v9, s[14:15]
	s_add_u32 s14, s14, 0x40000
	s_addc_u32 s15, s15, 0
	global_load_dword v22, v9, s[14:15]
	s_add_u32 s14, s14, 0x40000
	s_addc_u32 s15, s15, 0
	global_load_dword v23, v9, s[14:15]
	s_add_u32 s14, s14, 0x40000
	s_addc_u32 s15, s15, 0
	global_load_dword v24, v9, s[14:15]
	s_add_u32 s14, s14, 0x40000
	s_addc_u32 s15, s15, 0
	global_load_dword v25, v9, s[14:15]
	s_add_u32 s14, s14, 0x40000
	s_addc_u32 s15, s15, 0
	global_load_dword v26, v9, s[14:15]
	s_add_u32 s14, s14, 0x40000
	s_addc_u32 s15, s15, 0
	global_load_dword v27, v9, s[14:15]
	s_add_u32 s14, s14, 0x40000
	s_addc_u32 s15, s15, 0
	global_load_dword v28, v9, s[14:15]
	s_add_u32 s14, s14, 0x40000
	s_addc_u32 s15, s15, 0
	global_load_dword v29, v9, s[14:15]
	s_add_u32 s14, s14, 0x40000
	s_addc_u32 s15, s15, 0
	global_load_dword v30, v9, s[14:15]
	s_add_u32 s14, s14, 0x40000
	s_addc_u32 s15, s15, 0
	global_load_dword v31, v9, s[14:15]
	s_add_u32 s14, s14, 0x40000
	s_addc_u32 s15, s15, 0
	global_load_dword v32, v9, s[14:15]
	s_add_u32 s14, s14, 0x40000
	s_addc_u32 s15, s15, 0
	global_load_dword v33, v9, s[14:15]
	s_add_u32 s14, s14, 0x40000
	s_addc_u32 s15, s15, 0
	global_load_dword v34, v9, s[14:15]
	s_add_u32 s14, s14, 0x40000
	s_addc_u32 s15, s15, 0
	global_load_dword v35, v9, s[14:15]
	s_add_u32 s14, s14, 0x40000
	s_addc_u32 s15, s15, 0
.Lrs_last:
	v_bfe_u32 v16, v13, 16, 1
	v_bfe_u32 v17, v12, 16, 1
	v_add3_u32 v16, v13, v16, s12
	v_add3_u32 v17, v12, v17, s12
	v_lshrrev_b32_e32 v16, 16, v16
	v_and_or_b32 v16, v17, s13, v16
	global_store_dword v9, v16, s[16:17]
	s_add_u32 s16, s16, 0x40000
	s_addc_u32 s17, s17, 0
	s_waitcnt vmcnt(32)
	v_lshlrev_b32_e32 v19, 16, v36
	v_and_b32_e32 v18, 0xffff0000, v36
	v_pk_fma_f32 v[12:13], v[6:7], v[12:13], v[18:19]
	v_bfe_u32 v10, v13, 16, 1
	v_bfe_u32 v11, v12, 16, 1
	v_add3_u32 v10, v13, v10, s12
	v_add3_u32 v11, v12, v11, s12
	v_lshrrev_b32_e32 v10, 16, v10
	v_and_or_b32 v10, v11, s13, v10
	global_store_dword v9, v10, s[16:17]
	s_add_u32 s16, s16, 0x40000
	s_addc_u32 s17, s17, 0
	s_waitcnt vmcnt(32)
	v_lshlrev_b32_e32 v19, 16, v37
	v_and_b32_e32 v18, 0xffff0000, v37
	v_pk_fma_f32 v[12:13], v[6:7], v[12:13], v[18:19]
	v_bfe_u32 v16, v13, 16, 1
	v_bfe_u32 v17, v12, 16, 1
	v_add3_u32 v16, v13, v16, s12
	v_add3_u32 v17, v12, v17, s12
	v_lshrrev_b32_e32 v16, 16, v16
	v_and_or_b32 v16, v17, s13, v16
	global_store_dword v9, v16, s[16:17]
	s_add_u32 s16, s16, 0x40000
	s_addc_u32 s17, s17, 0
	s_waitcnt vmcnt(32)
	v_lshlrev_b32_e32 v19, 16, v38
	v_and_b32_e32 v18, 0xffff0000, v38
	v_pk_fma_f32 v[12:13], v[6:7], v[12:13], v[18:19]
	v_bfe_u32 v10, v13, 16, 1
	v_bfe_u32 v11, v12, 16, 1
	v_add3_u32 v10, v13, v10, s12
	v_add3_u32 v11, v12, v11, s12
	v_lshrrev_b32_e32 v10, 16, v10
	v_and_or_b32 v10, v11, s13, v10
	global_store_dword v9, v10, s[16:17]
	s_add_u32 s16, s16, 0x40000
	s_addc_u32 s17, s17, 0
	s_waitcnt vmcnt(32)
	v_lshlrev_b32_e32 v19, 16, v39
	v_and_b32_e32 v18, 0xffff0000, v39
	v_pk_fma_f32 v[12:13], v[6:7], v[12:13], v[18:19]
	v_bfe_u32 v16, v13, 16, 1
	v_bfe_u32 v17, v12, 16, 1
	v_add3_u32 v16, v13, v16, s12
	v_add3_u32 v17, v12, v17, s12
	v_lshrrev_b32_e32 v16, 16, v16
	v_and_or_b32 v16, v17, s13, v16
	global_store_dword v9, v16, s[16:17]
	s_add_u32 s16, s16, 0x40000
	s_addc_u32 s17, s17, 0
	s_waitcnt vmcnt(32)
	v_lshlrev_b32_e32 v19, 16, v40
	v_and_b32_e32 v18, 0xffff0000, v40
	v_pk_fma_f32 v[12:13], v[6:7], v[12:13], v[18:19]
	v_bfe_u32 v10, v13, 16, 1
	v_bfe_u32 v11, v12, 16, 1
	v_add3_u32 v10, v13, v10, s12
	v_add3_u32 v11, v12, v11, s12
	v_lshrrev_b32_e32 v10, 16, v10
	v_and_or_b32 v10, v11, s13, v10
	global_store_dword v9, v10, s[16:17]
	s_add_u32 s16, s16, 0x40000
	s_addc_u32 s17, s17, 0
	s_waitcnt vmcnt(32)
	v_lshlrev_b32_e32 v19, 16, v41
	v_and_b32_e32 v18, 0xffff0000, v41
	v_pk_fma_f32 v[12:13], v[6:7], v[12:13], v[18:19]
	v_bfe_u32 v16, v13, 16, 1
	v_bfe_u32 v17, v12, 16, 1
	v_add3_u32 v16, v13, v16, s12
	v_add3_u32 v17, v12, v17, s12
	v_lshrrev_b32_e32 v16, 16, v16
	v_and_or_b32 v16, v17, s13, v16
	global_store_dword v9, v16, s[16:17]
	s_add_u32 s16, s16, 0x40000
	s_addc_u32 s17, s17, 0
	s_waitcnt vmcnt(32)
	v_lshlrev_b32_e32 v19, 16, v42
	v_and_b32_e32 v18, 0xffff0000, v42
	v_pk_fma_f32 v[12:13], v[6:7], v[12:13], v[18:19]
	v_bfe_u32 v10, v13, 16, 1
	v_bfe_u32 v11, v12, 16, 1
	v_add3_u32 v10, v13, v10, s12
	v_add3_u32 v11, v12, v11, s12
	v_lshrrev_b32_e32 v10, 16, v10
	v_and_or_b32 v10, v11, s13, v10
	global_store_dword v9, v10, s[16:17]
	s_add_u32 s16, s16, 0x40000
	s_addc_u32 s17, s17, 0
	s_waitcnt vmcnt(32)
	v_lshlrev_b32_e32 v19, 16, v43
	v_and_b32_e32 v18, 0xffff0000, v43
	v_pk_fma_f32 v[12:13], v[6:7], v[12:13], v[18:19]
	v_bfe_u32 v16, v13, 16, 1
	v_bfe_u32 v17, v12, 16, 1
	v_add3_u32 v16, v13, v16, s12
	v_add3_u32 v17, v12, v17, s12
	v_lshrrev_b32_e32 v16, 16, v16
	v_and_or_b32 v16, v17, s13, v16
	global_store_dword v9, v16, s[16:17]
	s_add_u32 s16, s16, 0x40000
	s_addc_u32 s17, s17, 0
	s_waitcnt vmcnt(32)
	v_lshlrev_b32_e32 v19, 16, v44
	v_and_b32_e32 v18, 0xffff0000, v44
	v_pk_fma_f32 v[12:13], v[6:7], v[12:13], v[18:19]
	v_bfe_u32 v10, v13, 16, 1
	v_bfe_u32 v11, v12, 16, 1
	v_add3_u32 v10, v13, v10, s12
	v_add3_u32 v11, v12, v11, s12
	v_lshrrev_b32_e32 v10, 16, v10
	v_and_or_b32 v10, v11, s13, v10
	global_store_dword v9, v10, s[16:17]
	s_add_u32 s16, s16, 0x40000
	s_addc_u32 s17, s17, 0
	s_waitcnt vmcnt(32)
	v_lshlrev_b32_e32 v19, 16, v45
	v_and_b32_e32 v18, 0xffff0000, v45
	v_pk_fma_f32 v[12:13], v[6:7], v[12:13], v[18:19]
	v_bfe_u32 v16, v13, 16, 1
	v_bfe_u32 v17, v12, 16, 1
	v_add3_u32 v16, v13, v16, s12
	v_add3_u32 v17, v12, v17, s12
	v_lshrrev_b32_e32 v16, 16, v16
	v_and_or_b32 v16, v17, s13, v16
	global_store_dword v9, v16, s[16:17]
	s_add_u32 s16, s16, 0x40000
	s_addc_u32 s17, s17, 0
	s_waitcnt vmcnt(32)
	v_lshlrev_b32_e32 v19, 16, v46
	v_and_b32_e32 v18, 0xffff0000, v46
	v_pk_fma_f32 v[12:13], v[6:7], v[12:13], v[18:19]
	v_bfe_u32 v10, v13, 16, 1
	v_bfe_u32 v11, v12, 16, 1
	v_add3_u32 v10, v13, v10, s12
	v_add3_u32 v11, v12, v11, s12
	v_lshrrev_b32_e32 v10, 16, v10
	v_and_or_b32 v10, v11, s13, v10
	global_store_dword v9, v10, s[16:17]
	s_add_u32 s16, s16, 0x40000
	s_addc_u32 s17, s17, 0
	s_waitcnt vmcnt(32)
	v_lshlrev_b32_e32 v19, 16, v47
	v_and_b32_e32 v18, 0xffff0000, v47
	v_pk_fma_f32 v[12:13], v[6:7], v[12:13], v[18:19]
	v_bfe_u32 v16, v13, 16, 1
	v_bfe_u32 v17, v12, 16, 1
	v_add3_u32 v16, v13, v16, s12
	v_add3_u32 v17, v12, v17, s12
	v_lshrrev_b32_e32 v16, 16, v16
	v_and_or_b32 v16, v17, s13, v16
	global_store_dword v9, v16, s[16:17]
	s_add_u32 s16, s16, 0x40000
	s_addc_u32 s17, s17, 0
	s_waitcnt vmcnt(32)
	v_lshlrev_b32_e32 v19, 16, v48
	v_and_b32_e32 v18, 0xffff0000, v48
	v_pk_fma_f32 v[12:13], v[6:7], v[12:13], v[18:19]
	v_bfe_u32 v10, v13, 16, 1
	v_bfe_u32 v11, v12, 16, 1
	v_add3_u32 v10, v13, v10, s12
	v_add3_u32 v11, v12, v11, s12
	v_lshrrev_b32_e32 v10, 16, v10
	v_and_or_b32 v10, v11, s13, v10
	global_store_dword v9, v10, s[16:17]
	s_add_u32 s16, s16, 0x40000
	s_addc_u32 s17, s17, 0
	s_waitcnt vmcnt(32)
	v_lshlrev_b32_e32 v19, 16, v49
	v_and_b32_e32 v18, 0xffff0000, v49
	v_pk_fma_f32 v[12:13], v[6:7], v[12:13], v[18:19]
	v_bfe_u32 v16, v13, 16, 1
	v_bfe_u32 v17, v12, 16, 1
	v_add3_u32 v16, v13, v16, s12
	v_add3_u32 v17, v12, v17, s12
	v_lshrrev_b32_e32 v16, 16, v16
	v_and_or_b32 v16, v17, s13, v16
	global_store_dword v9, v16, s[16:17]
	s_add_u32 s16, s16, 0x40000
	s_addc_u32 s17, s17, 0
	s_waitcnt vmcnt(32)
	v_lshlrev_b32_e32 v19, 16, v50
	v_and_b32_e32 v18, 0xffff0000, v50
	v_pk_fma_f32 v[12:13], v[6:7], v[12:13], v[18:19]
	v_bfe_u32 v10, v13, 16, 1
	v_bfe_u32 v11, v12, 16, 1
	v_add3_u32 v10, v13, v10, s12
	v_add3_u32 v11, v12, v11, s12
	v_lshrrev_b32_e32 v10, 16, v10
	v_and_or_b32 v10, v11, s13, v10
	global_store_dword v9, v10, s[16:17]
	s_add_u32 s16, s16, 0x40000
	s_addc_u32 s17, s17, 0
	s_waitcnt vmcnt(32)
	v_lshlrev_b32_e32 v19, 16, v51
	v_and_b32_e32 v18, 0xffff0000, v51
	v_pk_fma_f32 v[12:13], v[6:7], v[12:13], v[18:19]
	s_add_i32 s8, s8, 1
	s_cmp_eq_u32 s8, 4
	s_cbranch_scc0 .Lrs_loop
	v_add_u32_e32 v194, s30, v194
	v_cmp_lt_i32_e32 vcc, s29, v194
	v_lshl_add_u64 v[2:3], v[2:3], 0, s[2:3]
	s_or_b64 s[6:7], vcc, s[6:7]
	v_lshl_add_u64 v[4:5], v[4:5], 0, s[2:3]
	s_andn2_b64 exec, exec, s[6:7]
	s_cbranch_execnz .LBB0_526
